# stack29 = stack23 + neighbourhood-attention softmax: 27 pairs of scalar score-minus-max subtractions merged into packed v_pk_add_f32
# speedup vs baseline: 1.0015x; 1.0015x over previous
; DEVINL unsigned pk2(float lo, float hi) { const f32x2 v = {lo, hi}; return __builtin_bit_cast(unsigned, __builtin_convertvector(v, bf16v2)); }
; DEVINL void phase3(const Params& P, unsigned char* smem) {
;     ...
;             float sum = 0.f;
;             bf16x8 pf[8];
; #pragma unroll
;             for (int kk = 0; kk < 8; ++kk) {
;                 float pe[8];
; #pragma unroll
;                 for (int e = 0; e < 4; ++e) { pe[e] = __builtin_amdgcn_exp2f(sc[2 * kk][e] - mx); pe[4 + e] = __builtin_amdgcn_exp2f(sc[2 * kk + 1][e] - mx); }
;                 sum += ((pe[0] + pe[1]) + (pe[2] + pe[3])) + ((pe[4] + pe[5]) + (pe[6] + pe[7]));
;                 union { bf16x8 v; unsigned u[4]; } pk; pk.u[0] = pk2(pe[0], pe[1]); pk.u[1] = pk2(pe[2], pe[3]); pk.u[2] = pk2(pe[4], pe[5]); pk.u[3] = pk2(pe[6], pe[7]);
;                 pf[kk] = pk.v;
;             }
.LBB0_470:
	v_pk_add_f32 v[166:167], v[166:167], v[174:175] op_sel_hi:[1,0] neg_lo:[0,1] neg_hi:[0,1]
	v_pk_add_f32 v[168:169], v[168:169], v[174:175] op_sel_hi:[1,0] neg_lo:[0,1] neg_hi:[0,1]
	v_exp_f32_e32 v166, v166
	v_pk_add_f32 v[170:171], v[170:171], v[174:175] op_sel_hi:[1,0] neg_lo:[0,1] neg_hi:[0,1]
	v_exp_f32_e32 v167, v167
	v_exp_f32_e32 v168, v168
	v_exp_f32_e32 v169, v169
	v_pk_add_f32 v[158:159], v[158:159], v[174:175] op_sel_hi:[1,0] neg_lo:[0,1] neg_hi:[0,1]
	v_pk_add_f32 v[160:161], v[160:161], v[174:175] op_sel_hi:[1,0] neg_lo:[0,1] neg_hi:[0,1]
	v_exp_f32_e32 v170, v170
	v_exp_f32_e32 v171, v171
	v_exp_f32_e32 v158, v158
	v_pk_add_f32 v[162:163], v[162:163], v[174:175] op_sel_hi:[1,0] neg_lo:[0,1] neg_hi:[0,1]
	v_exp_f32_e32 v159, v159
	v_exp_f32_e32 v160, v160
	v_exp_f32_e32 v161, v161
	v_pk_add_f32 v[150:151], v[150:151], v[174:175] op_sel_hi:[1,0] neg_lo:[0,1] neg_hi:[0,1]
	v_pk_add_f32 v[152:153], v[152:153], v[174:175] op_sel_hi:[1,0] neg_lo:[0,1] neg_hi:[0,1]
	v_exp_f32_e32 v162, v162
	v_exp_f32_e32 v163, v163
	v_exp_f32_e32 v150, v150
	v_pk_add_f32 v[154:155], v[154:155], v[174:175] op_sel_hi:[1,0] neg_lo:[0,1] neg_hi:[0,1]
	v_exp_f32_e32 v151, v151
	v_exp_f32_e32 v152, v152
	v_exp_f32_e32 v153, v153
	v_pk_add_f32 v[142:143], v[142:143], v[174:175] op_sel_hi:[1,0] neg_lo:[0,1] neg_hi:[0,1]
	v_pk_add_f32 v[144:145], v[144:145], v[174:175] op_sel_hi:[1,0] neg_lo:[0,1] neg_hi:[0,1]
	v_pk_add_f32 v[172:173], v[172:173], v[174:175] op_sel_hi:[1,0] neg_lo:[0,1] neg_hi:[0,1]
	v_exp_f32_e32 v154, v154
	v_exp_f32_e32 v155, v155
	v_exp_f32_e32 v142, v142
	v_pk_add_f32 v[146:147], v[146:147], v[174:175] op_sel_hi:[1,0] neg_lo:[0,1] neg_hi:[0,1]
	v_exp_f32_e32 v143, v143
	v_exp_f32_e32 v144, v144
	v_exp_f32_e32 v145, v145
	v_pk_add_f32 v[134:135], v[134:135], v[174:175] op_sel_hi:[1,0] neg_lo:[0,1] neg_hi:[0,1]
	v_pk_add_f32 v[136:137], v[136:137], v[174:175] op_sel_hi:[1,0] neg_lo:[0,1] neg_hi:[0,1]
	v_exp_f32_e32 v172, v172
	v_exp_f32_e32 v173, v173
	v_add_f32_e32 v199, v166, v167
	v_add_f32_e32 v201, v168, v169
	v_pk_add_f32 v[164:165], v[164:165], v[174:175] op_sel_hi:[1,0] neg_lo:[0,1] neg_hi:[0,1]
	v_exp_f32_e32 v146, v146
	v_exp_f32_e32 v147, v147
	v_exp_f32_e32 v134, v134
	v_pk_add_f32 v[138:139], v[138:139], v[174:175] op_sel_hi:[1,0] neg_lo:[0,1] neg_hi:[0,1]
	v_exp_f32_e32 v135, v135
	v_exp_f32_e32 v136, v136
	v_exp_f32_e32 v137, v137
	v_pk_add_f32 v[126:127], v[126:127], v[174:175] op_sel_hi:[1,0] neg_lo:[0,1] neg_hi:[0,1]
	v_pk_add_f32 v[128:129], v[128:129], v[174:175] op_sel_hi:[1,0] neg_lo:[0,1] neg_hi:[0,1]
	v_add_f32_e32 v199, v199, v201
	v_add_f32_e32 v201, v170, v171
	v_cvt_pk_bf16_f32 v166, v166, v167
	v_cvt_pk_bf16_f32 v167, v168, v169
	v_cvt_pk_bf16_f32 v168, v170, v171
	v_exp_f32_e32 v164, v164
	v_exp_f32_e32 v165, v165
	v_add_f32_e32 v170, v158, v159
	v_add_f32_e32 v171, v160, v161
	v_pk_add_f32 v[156:157], v[156:157], v[174:175] op_sel_hi:[1,0] neg_lo:[0,1] neg_hi:[0,1]
	v_exp_f32_e32 v138, v138
	v_exp_f32_e32 v139, v139
	v_exp_f32_e32 v126, v126
	v_pk_add_f32 v[130:131], v[130:131], v[174:175] op_sel_hi:[1,0] neg_lo:[0,1] neg_hi:[0,1]
	v_exp_f32_e32 v127, v127
	v_exp_f32_e32 v128, v128
	v_exp_f32_e32 v129, v129
	v_add_f32_e32 v170, v170, v171
	v_add_f32_e32 v171, v162, v163
	v_cvt_pk_bf16_f32 v158, v158, v159
	v_cvt_pk_bf16_f32 v159, v160, v161
	v_cvt_pk_bf16_f32 v160, v162, v163
	v_exp_f32_e32 v156, v156
	v_exp_f32_e32 v157, v157
	v_add_f32_e32 v162, v150, v151
	v_add_f32_e32 v163, v152, v153
	v_pk_add_f32 v[148:149], v[148:149], v[174:175] op_sel_hi:[1,0] neg_lo:[0,1] neg_hi:[0,1]
	v_exp_f32_e32 v130, v130
	v_exp_f32_e32 v131, v131
	v_add_f32_e32 v162, v162, v163
	v_add_f32_e32 v163, v154, v155
	v_cvt_pk_bf16_f32 v150, v150, v151
	v_cvt_pk_bf16_f32 v151, v152, v153
	v_cvt_pk_bf16_f32 v152, v154, v155
	v_exp_f32_e32 v148, v148
	v_exp_f32_e32 v149, v149
	v_add_f32_e32 v154, v142, v143
	v_add_f32_e32 v155, v144, v145
	v_pk_add_f32 v[140:141], v[140:141], v[174:175] op_sel_hi:[1,0] neg_lo:[0,1] neg_hi:[0,1]
	v_add_f32_e32 v224, v172, v173
	v_add_f32_e32 v154, v154, v155
	v_add_f32_e32 v155, v146, v147
	v_cvt_pk_bf16_f32 v142, v142, v143
	v_cvt_pk_bf16_f32 v143, v144, v145
	v_cvt_pk_bf16_f32 v144, v146, v147
	v_exp_f32_e32 v140, v140
	v_exp_f32_e32 v141, v141
	v_add_f32_e32 v146, v134, v135
	v_add_f32_e32 v147, v136, v137
	v_pk_add_f32 v[132:133], v[132:133], v[174:175] op_sel_hi:[1,0] neg_lo:[0,1] neg_hi:[0,1]
	v_add_f32_e32 v201, v201, v224
	v_cvt_pk_bf16_f32 v169, v172, v173
	v_add_f32_e32 v172, v164, v165
	v_add_f32_e32 v146, v146, v147
	v_add_f32_e32 v147, v138, v139
	v_cvt_pk_bf16_f32 v134, v134, v135
	v_cvt_pk_bf16_f32 v135, v136, v137
	v_cvt_pk_bf16_f32 v136, v138, v139
	v_exp_f32_e32 v132, v132
	v_exp_f32_e32 v133, v133
	v_add_f32_e32 v138, v126, v127
	v_add_f32_e32 v139, v128, v129
	v_pk_add_f32 v[118:119], v[118:119], v[174:175] op_sel_hi:[1,0] neg_lo:[0,1] neg_hi:[0,1]
	v_pk_add_f32 v[120:121], v[120:121], v[174:175] op_sel_hi:[1,0] neg_lo:[0,1] neg_hi:[0,1]
	v_sub_f32_e32 v124, v124, v174
	v_add_f32_e32 v199, v199, v201
	v_add_f32_e32 v171, v171, v172
	v_cvt_pk_bf16_f32 v161, v164, v165
	v_add_f32_e32 v164, v156, v157
	v_add_f32_e32 v138, v138, v139
	v_add_f32_e32 v139, v130, v131
	v_cvt_pk_bf16_f32 v126, v126, v127
	v_cvt_pk_bf16_f32 v127, v128, v129
	v_cvt_pk_bf16_f32 v128, v130, v131
	v_exp_f32_e32 v118, v118
	v_pk_add_f32 v[122:123], v[122:123], v[174:175] op_sel_hi:[1,0] neg_lo:[0,1] neg_hi:[0,1]
	v_exp_f32_e32 v119, v119
	v_exp_f32_e32 v120, v120
	v_exp_f32_e32 v130, v124
	v_exp_f32_e32 v121, v121
	v_sub_f32_e32 v124, v125, v174
	v_add_f32_e32 v199, 0, v199
	v_add_f32_e32 v170, v170, v171
; DEVINL unsigned pk2(float lo, float hi) { const f32x2 v = {lo, hi}; return __builtin_bit_cast(unsigned, __builtin_convertvector(v, bf16v2)); }
; #define LAS3 __attribute__((address_space(3)))
; DEVINL void phase3(const Params& P, unsigned char* smem) {
;     ...
;             float sum = 0.f;
;             bf16x8 pf[8];
; #pragma unroll
;             for (int kk = 0; kk < 8; ++kk) {
;                 float pe[8];
; #pragma unroll
;                 for (int e = 0; e < 4; ++e) { pe[e] = __builtin_amdgcn_exp2f(sc[2 * kk][e] - mx); pe[4 + e] = __builtin_amdgcn_exp2f(sc[2 * kk + 1][e] - mx); }
;                 sum += ((pe[0] + pe[1]) + (pe[2] + pe[3])) + ((pe[4] + pe[5]) + (pe[6] + pe[7]));
;                 union { bf16x8 v; unsigned u[4]; } pk; pk.u[0] = pk2(pe[0], pe[1]); pk.u[1] = pk2(pe[2], pe[3]); pk.u[2] = pk2(pe[4], pe[5]); pk.u[3] = pk2(pe[6], pe[7]);
;                 pf[kk] = pk.v;
;             }
;             sum = gsum4(sum);
;             f32x4 o[4];
; #pragma unroll
;             for (int dt = 0; dt < 4; ++dt) o[dt] = (f32x4){0.f, 0.f, 0.f, 0.f};
;             const int vrow = kc0 + 4 * g + (lr >> 2), vsw = (vrow >> 1) & 3, vbase = VR + vrow * 128 + (lr & 3) * 8;
; #pragma unroll
;             for (int kk = 0; kk < 8; ++kk) {
;                 const int sl = ((r0 + kk) % 9) * 8192;
; #pragma unroll
;                 for (int dt = 0; dt < 4; ++dt) {
;                     const LAS3 unsigned char* ap = lsm + vbase + sl + ((dt ^ vsw) << 5);
;                     o[dt] = __builtin_amdgcn_mfma_f32_16x16x32_bf16(tr_pair(ap, ap + 2048), pf[kk], o[dt], 0, 0, 0);
;                 }
;             }
	v_add_f32_e32 v163, v163, v164
	v_cvt_pk_bf16_f32 v153, v156, v157
	v_add_f32_e32 v156, v148, v149
	v_exp_f32_e32 v122, v122
	v_exp_f32_e32 v123, v123
	v_exp_f32_e32 v131, v124
	v_add_f32_e32 v170, v170, v199
	v_add_f32_e32 v162, v162, v163
	v_add_f32_e32 v155, v155, v156
	v_cvt_pk_bf16_f32 v145, v148, v149
	v_add_f32_e32 v148, v140, v141
	v_add_f32_e32 v162, v162, v170
	v_add_f32_e32 v154, v154, v155
	v_add_f32_e32 v147, v147, v148
	v_cvt_pk_bf16_f32 v137, v140, v141
	v_add_f32_e32 v140, v132, v133
	v_add_f32_e32 v154, v154, v162
	v_add_f32_e32 v146, v146, v147
	v_add_f32_e32 v139, v139, v140
	v_add_f32_e32 v124, v118, v119
	v_add_f32_e32 v125, v120, v121
	v_add_f32_e32 v146, v146, v154
	v_add_f32_e32 v138, v138, v139
	v_cvt_pk_bf16_f32 v129, v132, v133
	v_add_f32_e32 v124, v124, v125
	v_add_f32_e32 v125, v122, v123
	v_add_f32_e32 v132, v130, v131
	v_add_f32_e32 v138, v138, v146
	v_add_f32_e32 v125, v125, v132
	v_add_u32_e32 v146, s92, v189
	v_add_f32_e32 v124, v124, v125
	v_cvt_pk_bf16_f32 v118, v118, v119
	v_cvt_pk_bf16_f32 v119, v120, v121
	v_add_u32_e32 v121, v146, v220
	v_sub_f32_e32 v110, v110, v174
	v_add_f32_e32 v170, v124, v138
	v_cvt_pk_bf16_f32 v120, v122, v123
	ds_read_b64_tr_b16 v[122:123], v121
	ds_read_b64_tr_b16 v[124:125], v121 offset:2048
	v_add_u32_e32 v132, v146, v221
	v_exp_f32_e32 v172, v110
	v_add_u32_e32 v110, v146, v222
	v_cvt_pk_bf16_f32 v121, v130, v131
	ds_read_b64_tr_b16 v[130:131], v132
	ds_read_b64_tr_b16 v[132:133], v132 offset:2048
	ds_read_b64_tr_b16 v[138:139], v110
	ds_read_b64_tr_b16 v[140:141], v110 offset:2048
	v_add_u32_e32 v110, v146, v223
	v_sub_f32_e32 v114, v114, v174
	ds_read_b64_tr_b16 v[146:147], v110
	ds_read_b64_tr_b16 v[148:149], v110 offset:2048
	v_add_u32_e32 v110, s88, v189
	v_exp_f32_e32 v171, v114
	v_add_u32_e32 v114, v110, v220
	ds_read_b64_tr_b16 v[154:155], v114
	ds_read_b64_tr_b16 v[156:157], v114 offset:2048
	s_waitcnt lgkmcnt(8)
	v_mfma_f32_16x16x32_bf16 v[122:125], v[122:125], v[166:169], 0
	v_add_u32_e32 v114, v110, v221
	ds_read_b64_tr_b16 v[162:163], v114
	ds_read_b64_tr_b16 v[164:165], v114 offset:2048
	v_sub_f32_e32 v114, v115, v174
	s_waitcnt lgkmcnt(8)
	v_mfma_f32_16x16x32_bf16 v[130:133], v[130:133], v[166:169], 0
	v_exp_f32_e32 v173, v114
	v_add_u32_e32 v114, v110, v222
	v_add_u32_e32 v110, v110, v223
	s_waitcnt lgkmcnt(2)
	v_mfma_f32_16x16x32_bf16 v[122:125], v[154:157], v[158:161], v[122:125]
	ds_read_b64_tr_b16 v[154:155], v114
	ds_read_b64_tr_b16 v[156:157], v114 offset:2048
	v_sub_f32_e32 v111, v111, v174
	v_exp_f32_e32 v199, v111
	v_mfma_f32_16x16x32_bf16 v[138:141], v[138:141], v[166:169], 0
	v_sub_f32_e32 v111, v116, v174
	v_exp_f32_e32 v201, v111
	s_and_b64 s[48:49], s[48:49], s[38:39]
	s_waitcnt lgkmcnt(2)
	v_mfma_f32_16x16x32_bf16 v[130:133], v[162:165], v[158:161], v[130:133]
	ds_read_b64_tr_b16 v[162:163], v110
	ds_read_b64_tr_b16 v[164:165], v110 offset:2048
	v_add_u32_e32 v110, s91, v189
	v_add_u32_e32 v114, v110, v220
	v_mfma_f32_16x16x32_bf16 v[146:149], v[146:149], v[166:169], 0
	ds_read_b64_tr_b16 v[166:167], v114
	ds_read_b64_tr_b16 v[168:169], v114 offset:2048
	v_add_u32_e32 v114, v110, v221
	v_add_u32_e32 v111, v110, v222
	s_waitcnt lgkmcnt(4)
	v_mfma_f32_16x16x32_bf16 v[138:141], v[154:157], v[158:161], v[138:141]
	ds_read_b64_tr_b16 v[154:155], v114
	ds_read_b64_tr_b16 v[156:157], v114 offset:2048
	v_add_u32_e32 v110, v110, v223
	s_and_b64 s[48:49], s[48:49], s[36:37]
	s_waitcnt lgkmcnt(4)
	v_mfma_f32_16x16x32_bf16 v[146:149], v[162:165], v[158:161], v[146:149]
	ds_read_b64_tr_b16 v[158:159], v111
	ds_read_b64_tr_b16 v[160:161], v111 offset:2048
	s_andn2_b64 vcc, exec, s[48:49]
	s_waitcnt lgkmcnt(2)
	v_mfma_f32_16x16x32_bf16 v[130:133], v[154:157], v[150:153], v[130:133]
	ds_read_b64_tr_b16 v[154:155], v110
	ds_read_b64_tr_b16 v[156:157], v110 offset:2048
	v_add_u32_e32 v110, s90, v189
	v_add_u32_e32 v111, v110, v220
	ds_read_b64_tr_b16 v[162:163], v111
	ds_read_b64_tr_b16 v[164:165], v111 offset:2048
	v_add_u32_e32 v111, v110, v221
	s_waitcnt lgkmcnt(4)
	v_mfma_f32_16x16x32_bf16 v[138:141], v[158:161], v[150:153], v[138:141]
	ds_read_b64_tr_b16 v[158:159], v111
	ds_read_b64_tr_b16 v[160:161], v111 offset:2048
	v_sub_f32_e32 v111, v112, v174
	v_add_u32_e32 v112, v110, v222
	v_mfma_f32_16x16x32_bf16 v[122:125], v[166:169], v[150:153], v[122:125]
	v_add_u32_e32 v110, v110, v223
	v_exp_f32_e32 v166, v111
	v_sub_f32_e32 v111, v117, v174
	s_waitcnt lgkmcnt(0)
	v_mfma_f32_16x16x32_bf16 v[130:133], v[158:161], v[142:145], v[130:133]
	v_add_u32_e32 v158, s89, v189
	v_mfma_f32_16x16x32_bf16 v[146:149], v[154:157], v[150:153], v[146:149]
	v_mfma_f32_16x16x32_bf16 v[114:117], v[162:165], v[142:145], v[122:125]
	s_nop 2
	ds_read_b64_tr_b16 v[122:123], v112
	ds_read_b64_tr_b16 v[124:125], v112 offset:2048
	ds_read_b64_tr_b16 v[150:151], v110
	ds_read_b64_tr_b16 v[152:153], v110 offset:2048
	v_add_u32_e32 v110, v158, v220
	ds_read_b64_tr_b16 v[154:155], v110
	ds_read_b64_tr_b16 v[156:157], v110 offset:2048
	v_add_u32_e32 v110, v158, v221
	s_waitcnt lgkmcnt(4)
; #define LAS3 __attribute__((address_space(3)))
; DEVINL void phase3(const Params& P, unsigned char* smem) {
;     ...
;             f32x4 o[4];
; #pragma unroll
;             for (int dt = 0; dt < 4; ++dt) o[dt] = (f32x4){0.f, 0.f, 0.f, 0.f};
;             const int vrow = kc0 + 4 * g + (lr >> 2), vsw = (vrow >> 1) & 3, vbase = VR + vrow * 128 + (lr & 3) * 8;
; #pragma unroll
;             for (int kk = 0; kk < 8; ++kk) {
;                 const int sl = ((r0 + kk) % 9) * 8192;
; #pragma unroll
;                 for (int dt = 0; dt < 4; ++dt) {
;                     const LAS3 unsigned char* ap = lsm + vbase + sl + ((dt ^ vsw) << 5);
;                     o[dt] = __builtin_amdgcn_mfma_f32_16x16x32_bf16(tr_pair(ap, ap + 2048), pf[kk], o[dt], 0, 0, 0);
;                 }
;             }
;             if (p == 3 && it + G >= 2 * 8 * 16 && vb < 2 * 2 * 64 && !SKIPF(2048)) {
;                 const int sQ0 = (vb & 63) * 128, skvh = (vb >> 6) & 1, sb = vb >> 7;
;                 const bf16_t* sKg = (const bf16_t*)(P.ws + WS_SWK) + ((size_t)(sb * 2 + skvh) * SEQ) * 64;
; #pragma unroll
;                 for (int i = 0; i < 5; ++i) {
;                     const int idx = t + NTHR * i, kp = sQ0 - 128 + (idx >> 3), cch = idx & 7;
;                     const int tokk = kp < 0 ? 0 : (kp > SEQ - 1 ? SEQ - 1 : kp);
;                     swk[i] = *(const u32x4*)(sKg + (size_t)tokk * 64 + cch * 8);
;                 }
	v_mfma_f32_16x16x32_bf16 v[122:125], v[122:125], v[142:145], v[138:141]
	s_nop 2
	ds_read_b64_tr_b16 v[138:139], v110
	ds_read_b64_tr_b16 v[140:141], v110 offset:2048
	v_sub_f32_e32 v110, v113, v174
	s_waitcnt lgkmcnt(4)
	v_mfma_f32_16x16x32_bf16 v[142:145], v[150:153], v[142:145], v[146:149]
	v_exp_f32_e32 v150, v111
	v_exp_f32_e32 v151, v110
	v_add_u32_e32 v152, s87, v189
	s_waitcnt lgkmcnt(2)
	v_mfma_f32_16x16x32_bf16 v[110:113], v[154:157], v[134:137], v[114:117]
	v_add_u32_e32 v148, v152, v220
	s_nop 1
	v_add_u32_e32 v116, v158, v222
	ds_read_b64_tr_b16 v[114:115], v116
	ds_read_b64_tr_b16 v[116:117], v116 offset:2048
	s_waitcnt lgkmcnt(2)
	v_mfma_f32_16x16x32_bf16 v[130:133], v[138:141], v[134:137], v[130:133]
	v_add_u32_e32 v140, v158, v223
	ds_read_b64_tr_b16 v[138:139], v140
	ds_read_b64_tr_b16 v[140:141], v140 offset:2048
	ds_read_b64_tr_b16 v[146:147], v148
	ds_read_b64_tr_b16 v[148:149], v148 offset:2048
	s_waitcnt lgkmcnt(4)
	v_mfma_f32_16x16x32_bf16 v[114:117], v[114:117], v[134:137], v[122:125]
	s_nop 2
	v_add_u32_e32 v124, v152, v221
	ds_read_b64_tr_b16 v[122:123], v124
	ds_read_b64_tr_b16 v[124:125], v124 offset:2048
	s_waitcnt lgkmcnt(4)
	v_mfma_f32_16x16x32_bf16 v[134:137], v[138:141], v[134:137], v[142:145]
	v_add_u32_e32 v140, v152, v222
	ds_read_b64_tr_b16 v[138:139], v140
	ds_read_b64_tr_b16 v[140:141], v140 offset:2048
	v_add_f32_e32 v142, v171, v173
	s_waitcnt lgkmcnt(2)
	v_mfma_f32_16x16x32_bf16 v[122:125], v[122:125], v[126:129], v[130:133]
	v_add_f32_e32 v143, v201, v150
	v_add_f32_e32 v142, v142, v143
	v_add_u32_e32 v143, s86, v189
	v_add_u32_e32 v132, v152, v223
	ds_read_b64_tr_b16 v[130:131], v132
	ds_read_b64_tr_b16 v[132:133], v132 offset:2048
	v_mfma_f32_16x16x32_bf16 v[110:113], v[146:149], v[126:129], v[110:113]
	v_add_u32_e32 v147, s67, v189
	v_add_f32_e32 v144, v172, v199
	v_add_f32_e32 v145, v166, v151
	s_waitcnt lgkmcnt(2)
	v_mfma_f32_16x16x32_bf16 v[114:117], v[138:141], v[126:129], v[114:117]
	v_add_u32_e32 v140, v143, v220
	ds_read_b64_tr_b16 v[138:139], v140
	ds_read_b64_tr_b16 v[140:141], v140 offset:2048
	v_add_f32_e32 v144, v144, v145
	s_waitcnt lgkmcnt(2)
	v_mfma_f32_16x16x32_bf16 v[126:129], v[130:133], v[126:129], v[134:137]
	v_add_u32_e32 v132, v143, v221
	ds_read_b64_tr_b16 v[130:131], v132
	ds_read_b64_tr_b16 v[132:133], v132 offset:2048
	v_add_u32_e32 v136, v143, v222
	ds_read_b64_tr_b16 v[134:135], v136
	ds_read_b64_tr_b16 v[136:137], v136 offset:2048
	s_waitcnt lgkmcnt(2)
	v_mfma_f32_16x16x32_bf16 v[122:125], v[130:133], v[118:121], v[122:125]
	v_add_u32_e32 v132, v143, v223
	ds_read_b64_tr_b16 v[130:131], v132
	ds_read_b64_tr_b16 v[132:133], v132 offset:2048
	v_add_f32_e32 v142, v142, v144
	s_waitcnt lgkmcnt(2)
	v_mfma_f32_16x16x32_bf16 v[114:117], v[134:137], v[118:121], v[114:117]
	v_add_u32_e32 v136, v147, v220
	ds_read_b64_tr_b16 v[134:135], v136
	ds_read_b64_tr_b16 v[136:137], v136 offset:2048
	v_add_f32_e32 v146, v142, v170
	v_mfma_f32_16x16x32_bf16 v[110:113], v[138:141], v[118:121], v[110:113]
	v_cvt_pk_bf16_f32 v138, v171, v173
	v_cvt_pk_bf16_f32 v139, v201, v150
	v_cvt_pk_bf16_f32 v140, v172, v199
	v_cvt_pk_bf16_f32 v141, v166, v151
	s_waitcnt lgkmcnt(2)
	v_mfma_f32_16x16x32_bf16 v[128:131], v[130:133], v[118:121], v[126:129]
	v_add_u32_e32 v118, v147, v221
	ds_read_b64_tr_b16 v[142:143], v118
	ds_read_b64_tr_b16 v[144:145], v118 offset:2048
	v_mov_b32_e32 v148, v146
	s_waitcnt lgkmcnt(2)
	v_mfma_f32_16x16x32_bf16 v[118:121], v[134:137], v[138:141], v[110:113]
	v_add_u32_e32 v134, v147, v223
	v_permlane16_swap_b32_e32 v146, v148
	s_nop 0
	v_add_u32_e32 v112, v147, v222
	ds_read_b64_tr_b16 v[110:111], v112
	ds_read_b64_tr_b16 v[112:113], v112 offset:2048
	ds_read_b64_tr_b16 v[132:133], v134
	ds_read_b64_tr_b16 v[134:135], v134 offset:2048
	s_waitcnt lgkmcnt(4)
	v_mfma_f32_16x16x32_bf16 v[122:125], v[142:145], v[138:141], v[122:125]
	v_add_f32_e32 v126, v146, v148
	v_mov_b32_e32 v127, v126
	s_nop 1
	v_permlane32_swap_b32_e32 v126, v127
	s_waitcnt lgkmcnt(2)
	v_mfma_f32_16x16x32_bf16 v[110:113], v[110:113], v[138:141], v[114:117]
	s_waitcnt lgkmcnt(0)
	v_mfma_f32_16x16x32_bf16 v[114:117], v[132:135], v[138:141], v[128:131]
	s_cbranch_vccnz .LBB0_472
	global_load_dwordx4 v[2:5], v[176:177], off
	global_load_dwordx4 v[6:9], v[178:179], off
	global_load_dwordx4 v[10:13], v[180:181], off
	global_load_dwordx4 v[14:17], v[182:183], off
	global_load_dwordx4 v[18:21], v[184:185], off
	s_mov_b64 s[46:47], -1
